# loop-edge rotation: mixer-B loop counter, exit test and ring rotation moved ahead of the loop-back barrier
# baseline (speedup 1.0000x reference)
; #define ATT_PK4(P, BASE, OUT) do { u32x4 w = {cvtpk(P[BASE + 0], P[BASE + 1]), cvtpk(P[BASE + 2], P[BASE + 3]), cvtpk(P[BASE + 4], P[BASE + 5]), cvtpk(P[BASE + 6], P[BASE + 7])}; \
;     OUT = *reinterpret_cast<bf16x8*>(&w); } while (0)
; __device__ __forceinline__ void softmax_exp_pack(f32x16& p0, f32x16& p1, bf16x8& pa0, bf16x8& pa1, bf16x8& pa2, bf16x8& pa3) {
;     ...
;   for (int r = 0; r < 16; ++r) { p0[r] = __builtin_amdgcn_exp2f(p0[r]); p1[r] = __builtin_amdgcn_exp2f(p1[r]); }
;     ...
;   ATT_PK4(p0, 0, pa0); ATT_PK4(p0, 8, pa1); ATT_PK4(p1, 0, pa2); ATT_PK4(p1, 8, pa3);
.Lrot_head_b1:
	v_cmp_ge_f32_e32 vcc, s60, v173
	s_cmp_eq_u64 vcc, exec
	s_cbranch_scc0 .LBB0_285
.LBB0_283:
	v_exp_f32_e32 v98, v98
	v_exp_f32_e32 v114, v114
	v_exp_f32_e32 v99, v99
	v_exp_f32_e32 v115, v115
	v_exp_f32_e32 v100, v100
	v_exp_f32_e32 v101, v101
	v_exp_f32_e32 v102, v102
	v_exp_f32_e32 v103, v103
	v_exp_f32_e32 v106, v106
	v_exp_f32_e32 v107, v107
	v_exp_f32_e32 v116, v116
	v_exp_f32_e32 v117, v117
	v_exp_f32_e32 v118, v118
	v_exp_f32_e32 v119, v119
	v_exp_f32_e32 v104, v104
	v_exp_f32_e32 v120, v120
	v_exp_f32_e32 v105, v105
	v_exp_f32_e32 v121, v121
	v_exp_f32_e32 v122, v122
	v_exp_f32_e32 v123, v123
	v_exp_f32_e32 v108, v108
	v_exp_f32_e32 v124, v124
	v_exp_f32_e32 v109, v109
	v_exp_f32_e32 v125, v125
	v_exp_f32_e32 v110, v110
	v_exp_f32_e32 v126, v126
	v_exp_f32_e32 v111, v111
	v_exp_f32_e32 v127, v127
	v_exp_f32_e32 v112, v112
	v_exp_f32_e32 v128, v128
	v_exp_f32_e32 v113, v113
	v_exp_f32_e32 v129, v129
	v_cvt_pk_bf16_f32 v2, v98, v99
	v_cvt_pk_bf16_f32 v3, v100, v101
	v_cvt_pk_bf16_f32 v4, v102, v103
	v_cvt_pk_bf16_f32 v6, v106, v107
	v_cvt_pk_bf16_f32 v10, v114, v115
	v_add_u32_e32 v114, s94, v169
	s_add_i32 s14, s95, 0
	s_waitcnt vmcnt(2)
	ds_write_b128 v114, v[224:227] offset:49152
	v_add_u32_e32 v114, s14, v167
	v_cvt_pk_bf16_f32 v5, v104, v105
	v_cvt_pk_bf16_f32 v7, v108, v109
	v_cvt_pk_bf16_f32 v8, v110, v111
	v_cvt_pk_bf16_f32 v9, v112, v113
	v_cvt_pk_bf16_f32 v11, v116, v117
	v_cvt_pk_bf16_f32 v12, v118, v119
	v_cvt_pk_bf16_f32 v13, v120, v121
	v_cvt_pk_bf16_f32 v14, v122, v123
	v_cvt_pk_bf16_f32 v15, v124, v125
	v_cvt_pk_bf16_f32 v16, v126, v127
	v_cvt_pk_bf16_f32 v17, v128, v129
	s_waitcnt vmcnt(1)
	ds_write_b128 v114, v[228:231]
	v_add_u32_e32 v114, s14, v168
	s_waitcnt vmcnt(0)
	ds_write_b128 v114, v[232:235]
	v_add_u32_e32 v249, s96, v172
	ds_read_b128 v[152:155], v249 offset:49152
	ds_read_b128 v[156:159], v249 offset:53760
	ds_read_b128 v[160:163], v249 offset:49184
	ds_read_b128 v[176:179], v249 offset:53792
	s_waitcnt lgkmcnt(4)
	s_barrier
; #define ATT_SBAR() __builtin_amdgcn_sched_barrier(0)
; __device__ __forceinline__ unsigned cvtpk(float lo, float hi) { f32x2_t v = {lo, hi}; bf16x2_t b = __builtin_convertvector(v, bf16x2_t); return __builtin_bit_cast(unsigned, b); }
; #define ATT_LOAD_K(t) do { const unsigned so_ = (unsigned)(t) * (unsigned)(KVBLK * LDK * 2); sk0 = __builtin_bit_cast(bf16x8, __builtin_amdgcn_raw_buffer_load_b128(krs, koff, so_, 0)); \
;     if constexpr (DQK == 128) sk1 = __builtin_bit_cast(bf16x8, __builtin_amdgcn_raw_buffer_load_b128(krs, koff, so_ + (unsigned)(32 * LDK * 2), 0)); } while (0)
; #define ATT_LOAD_V(t) do { const unsigned so_ = (unsigned)(t) * (unsigned)(KVBLK * LDV * 2); sv0 = __builtin_bit_cast(bf16x8, __builtin_amdgcn_raw_buffer_load_b128(vrs, voff, so_, 0)); \
;     sv1 = __builtin_bit_cast(bf16x8, __builtin_amdgcn_raw_buffer_load_b128(vrs, voff, so_ + (unsigned)(32 * LDV * 2), 0)); } while (0)
; #define ATT_WRITE_K(so) do { *(bf16x8*)(K_lds + (so) + kswz<DQK>(kr, kc * 2)) = sk0; if constexpr (DQK == 128) *(bf16x8*)(K_lds + (so) + kswz<DQK>(32 + kr, kc * 2)) = sk1; } while (0)
;     ...
;   for (int t = 0; t + 1 < NT; ++t) {
;     if constexpr (ABL & 1) { u32x4 w0 = {cvtpk(p0[0], p0[1]), cvtpk(p0[2], p0[3]), cvtpk(p0[4], p0[5]), cvtpk(p0[6], p0[7])}, w1 = {cvtpk(p0[8], p0[9]), cvtpk(p0[10], p0[11]), cvtpk(p0[12], p0[13]), cvtpk(p0[14], p0[15])};
;         u32x4 w2 = {cvtpk(p1[0], p1[1]), cvtpk(p1[2], p1[3]), cvtpk(p1[4], p1[5]), cvtpk(p1[6], p1[7])}, w3 = {cvtpk(p1[8], p1[9]), cvtpk(p1[10], p1[11]), cvtpk(p1[12], p1[13]), cvtpk(p1[14], p1[15])};
;         pa0 = *reinterpret_cast<bf16x8*>(&w0); pa1 = *reinterpret_cast<bf16x8*>(&w1); pa2 = *reinterpret_cast<bf16x8*>(&w2); pa3 = *reinterpret_cast<bf16x8*>(&w3); }
;     else { ATT_SOFTMAX(t == 0); }
;     if constexpr (!(ABL & 4)) { ATT_WRITE_K(k2); ATT_WRITE_V(v1); }
;     ATT_SBAR();
; #pragma unroll
;     for (int ks = 0; ks < 4; ++ks) ATT_VPAIR(va, v0, 0, ks);
;     asm volatile("s_waitcnt lgkmcnt(8)" ::: "memory"); ATT_BAR();
;     ATT_XSECTION(true);
;     if constexpr (!(ABL & 4)) { const int tk = (t + 3 < NT) ? t + 3 : NT - 1, tv = (t + 2 < NT) ? t + 2 : NT - 1; ATT_LOAD_K(tk); ATT_LOAD_V(tv); }
;     ATT_BAR();
;     { const int tk_ = k0; k0 = k1; k1 = k2; k2 = tk_; const int tv_ = v0; v0 = v1; v1 = v2; v2 = tv_; }
	s_setprio 2
	s_waitcnt lgkmcnt(3)
	v_mfma_f32_32x32x16_bf16 v[98:113], v[152:155], v[136:139], v[82:97]
	ds_read_b128 v[180:183], v249 offset:49216
	s_waitcnt lgkmcnt(3)
	v_mfma_f32_32x32x16_bf16 v[114:129], v[156:159], v[136:139], v[82:97]
	ds_read_b128 v[186:189], v249 offset:53824
	v_add_u32_e32 v248, s37, v131
	s_waitcnt lgkmcnt(3)
	v_mfma_f32_32x32x16_bf16 v[98:113], v[160:163], v[140:143], v[98:113]
	ds_read_b128 v[190:193], v249 offset:49248
	ds_read_b64_tr_b16 v[198:199], v248
	ds_read_b64_tr_b16 v[200:201], v248 offset:2048
	s_waitcnt lgkmcnt(5)
	v_mfma_f32_32x32x16_bf16 v[114:129], v[176:179], v[140:143], v[114:129]
	ds_read_b128 v[194:197], v249 offset:53856
	ds_read_b64_tr_b16 v[212:213], v248 offset:4096
	ds_read_b64_tr_b16 v[214:215], v248 offset:6144
	s_waitcnt lgkmcnt(7)
	v_mfma_f32_32x32x16_bf16 v[98:113], v[180:183], v[144:147], v[98:113]
	ds_read_b64_tr_b16 v[216:217], v248 offset:8192
	ds_read_b64_tr_b16 v[218:219], v248 offset:10240
	s_waitcnt lgkmcnt(8)
	v_mfma_f32_32x32x16_bf16 v[114:129], v[186:189], v[144:147], v[114:129]
	ds_read_b64_tr_b16 v[220:221], v248 offset:12288
	ds_read_b64_tr_b16 v[222:223], v248 offset:14336
	s_waitcnt lgkmcnt(9)
	v_mfma_f32_32x32x16_bf16 v[98:113], v[190:193], v[148:151], v[98:113]
	s_waitcnt lgkmcnt(6)
	v_mfma_f32_32x32x16_bf16 v[114:129], v[194:197], v[148:151], v[114:129]
	v_mfma_f32_32x32x16_bf16 v[18:33], v[2:5], v[198:201], v[18:33]
	ds_read_b64_tr_b16 v[236:237], v248 offset:512
	ds_read_b64_tr_b16 v[238:239], v248 offset:2560
	s_waitcnt lgkmcnt(6)
	v_mfma_f32_32x32x16_bf16 v[18:33], v[6:9], v[212:215], v[18:33]
	ds_read_b64_tr_b16 v[198:199], v248 offset:4608
	ds_read_b64_tr_b16 v[200:201], v248 offset:6656
	s_waitcnt lgkmcnt(6)
	v_mfma_f32_32x32x16_bf16 v[18:33], v[10:13], v[216:219], v[18:33]
	ds_read_b64_tr_b16 v[212:213], v248 offset:8704
	ds_read_b64_tr_b16 v[214:215], v248 offset:10752
	s_waitcnt lgkmcnt(6)
	v_mfma_f32_32x32x16_bf16 v[18:33], v[14:17], v[220:223], v[18:33]
	ds_read_b64_tr_b16 v[216:217], v248 offset:12800
	ds_read_b64_tr_b16 v[218:219], v248 offset:14848
	v_max3_f32 v249, v98, v99, v100
	s_waitcnt lgkmcnt(6)
	v_mfma_f32_32x32x16_bf16 v[34:49], v[2:5], v[236:239], v[34:49]
	ds_read_b64_tr_b16 v[220:221], v248 offset:1024
	ds_read_b64_tr_b16 v[222:223], v248 offset:3072
	v_max3_f32 v173, v114, v115, v116
	s_waitcnt lgkmcnt(6)
	v_mfma_f32_32x32x16_bf16 v[34:49], v[6:9], v[198:201], v[34:49]
	ds_read_b64_tr_b16 v[236:237], v248 offset:5120
	ds_read_b64_tr_b16 v[238:239], v248 offset:7168
	v_max3_f32 v249, v249, v101, v102
	s_waitcnt lgkmcnt(6)
	v_mfma_f32_32x32x16_bf16 v[34:49], v[10:13], v[212:215], v[34:49]
	ds_read_b64_tr_b16 v[198:199], v248 offset:9216
	ds_read_b64_tr_b16 v[200:201], v248 offset:11264
	v_max3_f32 v173, v173, v117, v118
	s_waitcnt lgkmcnt(6)
	v_mfma_f32_32x32x16_bf16 v[34:49], v[14:17], v[216:219], v[34:49]
	ds_read_b64_tr_b16 v[212:213], v248 offset:13312
	ds_read_b64_tr_b16 v[214:215], v248 offset:15360
	v_max3_f32 v249, v249, v103, v104
	s_waitcnt lgkmcnt(6)
	v_mfma_f32_32x32x16_bf16 v[50:65], v[2:5], v[220:223], v[50:65]
	ds_read_b64_tr_b16 v[216:217], v248 offset:1536
	ds_read_b64_tr_b16 v[218:219], v248 offset:3584
	v_max3_f32 v173, v173, v119, v120
	s_waitcnt lgkmcnt(6)
	v_mfma_f32_32x32x16_bf16 v[50:65], v[6:9], v[236:239], v[50:65]
	ds_read_b64_tr_b16 v[220:221], v248 offset:5632
	ds_read_b64_tr_b16 v[222:223], v248 offset:7680
	v_max3_f32 v249, v249, v105, v106
	s_waitcnt lgkmcnt(6)
	v_mfma_f32_32x32x16_bf16 v[50:65], v[10:13], v[198:201], v[50:65]
	ds_read_b64_tr_b16 v[236:237], v248 offset:9728
	ds_read_b64_tr_b16 v[238:239], v248 offset:11776
	v_max3_f32 v173, v173, v121, v122
	s_waitcnt lgkmcnt(6)
	v_mfma_f32_32x32x16_bf16 v[50:65], v[14:17], v[212:215], v[50:65]
	ds_read_b64_tr_b16 v[198:199], v248 offset:13824
	ds_read_b64_tr_b16 v[200:201], v248 offset:15872
	v_max3_f32 v249, v249, v107, v108
	s_waitcnt lgkmcnt(6)
	v_mfma_f32_32x32x16_bf16 v[66:81], v[2:5], v[216:219], v[66:81]
	v_max3_f32 v173, v173, v123, v124
	s_min_u32 s14, s97, 0x7c
	s_lshl_b32 s14, s14, 17
	s_add_i32 s14, s14, 0x60000
	buffer_load_dwordx4 v[224:227], v170, s[8:11], s14 offen
	s_waitcnt lgkmcnt(4)
	v_mfma_f32_32x32x16_bf16 v[66:81], v[6:9], v[220:223], v[66:81]
	v_max3_f32 v249, v249, v109, v110
	s_add_i32 s19, s36, 0xffff0000
	s_mov_b32 s14, s10
	s_mov_b32 s15, s11
	buffer_load_dwordx4 v[228:231], v171, s[12:15], s19 offen
	s_waitcnt lgkmcnt(2)
	v_mfma_f32_32x32x16_bf16 v[66:81], v[10:13], v[236:239], v[66:81]
	v_max3_f32 v173, v173, v125, v126
	buffer_load_dwordx4 v[232:235], v171, s[12:15], s36 offen
	s_waitcnt lgkmcnt(0)
	v_mfma_f32_32x32x16_bf16 v[66:81], v[14:17], v[198:201], v[66:81]
	v_max3_f32 v249, v249, v111, v112
	v_mfma_f32_4x4x4_16b_bf16 v[240:243], v[2:3], v[132:133], v[240:243]
	v_max3_f32 v173, v173, v127, v128
	v_mfma_f32_4x4x4_16b_bf16 v[244:247], v[4:5], v[132:133], v[244:247]
	v_mfma_f32_4x4x4_16b_bf16 v[240:243], v[6:7], v[132:133], v[240:243]
	v_max_f32 v249, v249, v113
	v_mfma_f32_4x4x4_16b_bf16 v[244:247], v[8:9], v[132:133], v[244:247]
	v_mfma_f32_4x4x4_16b_bf16 v[240:243], v[10:11], v[132:133], v[240:243]
	v_max_f32 v173, v173, v129
	v_mfma_f32_4x4x4_16b_bf16 v[244:247], v[12:13], v[132:133], v[244:247]
	v_mfma_f32_4x4x4_16b_bf16 v[240:243], v[14:15], v[132:133], v[240:243]
	v_max_f32 v173, v173, v249
	v_mfma_f32_4x4x4_16b_bf16 v[244:247], v[16:17], v[132:133], v[244:247]
	s_setprio 0
	s_add_i32 s36, s36, 0x20000
	s_add_i32 s97, s97, 1
	s_cmpk_eq_i32 s97, 0x7e
	s_cbranch_scc1 .Lrot_exit_b1
	s_mov_b32 s14, s94
	s_mov_b32 s94, s18
	s_mov_b32 s18, s96
	s_mov_b32 s15, s95
	s_mov_b32 s95, s93
	s_mov_b32 s93, s37
	s_mov_b32 s37, s15
	s_mov_b32 s96, s14
	s_barrier
	s_branch .Lrot_head_b1
.Lrot_exit_b1:
	s_barrier
	s_branch .LBB0_290

; #define ATT_PK4(P, BASE, OUT) do { u32x4 w = {cvtpk(P[BASE + 0], P[BASE + 1]), cvtpk(P[BASE + 2], P[BASE + 3]), cvtpk(P[BASE + 4], P[BASE + 5]), cvtpk(P[BASE + 6], P[BASE + 7])}; \
;     OUT = *reinterpret_cast<bf16x8*>(&w); } while (0)
; __device__ __forceinline__ void softmax_exp_pack(f32x16& p0, f32x16& p1, bf16x8& pa0, bf16x8& pa1, bf16x8& pa2, bf16x8& pa3) {
;     ...
;   for (int r = 0; r < 16; ++r) { p0[r] = __builtin_amdgcn_exp2f(p0[r]); p1[r] = __builtin_amdgcn_exp2f(p1[r]); }
;     ...
;   ATT_PK4(p0, 0, pa0); ATT_PK4(p0, 8, pa1); ATT_PK4(p1, 0, pa2); ATT_PK4(p1, 8, pa3);
.Lrot_head_b2:
	v_cmp_ge_f32_e32 vcc, s60, v174
	s_cmp_eq_u64 vcc, exec
	s_cbranch_scc0 .LBB0_300
.LBB0_298:
	v_exp_f32_e32 v98, v98
	v_exp_f32_e32 v114, v114
	v_exp_f32_e32 v99, v99
	v_exp_f32_e32 v115, v115
	v_exp_f32_e32 v100, v100
	v_exp_f32_e32 v101, v101
	v_exp_f32_e32 v102, v102
	v_exp_f32_e32 v103, v103
	v_exp_f32_e32 v106, v106
	v_exp_f32_e32 v107, v107
	v_exp_f32_e32 v116, v116
	v_exp_f32_e32 v117, v117
	v_exp_f32_e32 v118, v118
	v_exp_f32_e32 v119, v119
	v_exp_f32_e32 v104, v104
	v_exp_f32_e32 v120, v120
	v_exp_f32_e32 v105, v105
	v_exp_f32_e32 v121, v121
	v_exp_f32_e32 v122, v122
	v_exp_f32_e32 v123, v123
	v_exp_f32_e32 v108, v108
	v_exp_f32_e32 v124, v124
	v_exp_f32_e32 v109, v109
	v_exp_f32_e32 v125, v125
	v_exp_f32_e32 v110, v110
	v_exp_f32_e32 v126, v126
	v_exp_f32_e32 v111, v111
	v_exp_f32_e32 v127, v127
	v_exp_f32_e32 v112, v112
	v_exp_f32_e32 v128, v128
	v_exp_f32_e32 v113, v113
	v_exp_f32_e32 v129, v129
	v_cvt_pk_bf16_f32 v18, v98, v99
	v_cvt_pk_bf16_f32 v19, v100, v101
	v_cvt_pk_bf16_f32 v20, v102, v103
	v_cvt_pk_bf16_f32 v22, v106, v107
	v_cvt_pk_bf16_f32 v26, v114, v115
	v_add_u32_e32 v114, s49, v170
	s_add_i32 s14, s50, 0
	s_waitcnt vmcnt(2)
	ds_write_b128 v114, v[224:227] offset:49152
	v_add_u32_e32 v114, s14, v168
	v_cvt_pk_bf16_f32 v21, v104, v105
	v_cvt_pk_bf16_f32 v23, v108, v109
	v_cvt_pk_bf16_f32 v24, v110, v111
	v_cvt_pk_bf16_f32 v25, v112, v113
	v_cvt_pk_bf16_f32 v27, v116, v117
	v_cvt_pk_bf16_f32 v28, v118, v119
	v_cvt_pk_bf16_f32 v29, v120, v121
	v_cvt_pk_bf16_f32 v30, v122, v123
	v_cvt_pk_bf16_f32 v31, v124, v125
	v_cvt_pk_bf16_f32 v32, v126, v127
	v_cvt_pk_bf16_f32 v33, v128, v129
	s_waitcnt vmcnt(1)
	ds_write_b128 v114, v[228:231]
	v_add_u32_e32 v114, s14, v169
	s_waitcnt vmcnt(0)
	ds_write_b128 v114, v[232:235]
	v_add_u32_e32 v249, s18, v173
	ds_read_b128 v[152:155], v249 offset:49152
	ds_read_b128 v[156:159], v249 offset:53760
	ds_read_b128 v[160:163], v249 offset:49184
	ds_read_b128 v[176:179], v249 offset:53792
	s_waitcnt lgkmcnt(4)
	s_barrier
; #define ATT_SBAR() __builtin_amdgcn_sched_barrier(0)
; __device__ __forceinline__ unsigned cvtpk(float lo, float hi) { f32x2_t v = {lo, hi}; bf16x2_t b = __builtin_convertvector(v, bf16x2_t); return __builtin_bit_cast(unsigned, b); }
; #define ATT_LOAD_K(t) do { const unsigned so_ = (unsigned)(t) * (unsigned)(KVBLK * LDK * 2); sk0 = __builtin_bit_cast(bf16x8, __builtin_amdgcn_raw_buffer_load_b128(krs, koff, so_, 0)); \
;     if constexpr (DQK == 128) sk1 = __builtin_bit_cast(bf16x8, __builtin_amdgcn_raw_buffer_load_b128(krs, koff, so_ + (unsigned)(32 * LDK * 2), 0)); } while (0)
; #define ATT_LOAD_V(t) do { const unsigned so_ = (unsigned)(t) * (unsigned)(KVBLK * LDV * 2); sv0 = __builtin_bit_cast(bf16x8, __builtin_amdgcn_raw_buffer_load_b128(vrs, voff, so_, 0)); \
;     sv1 = __builtin_bit_cast(bf16x8, __builtin_amdgcn_raw_buffer_load_b128(vrs, voff, so_ + (unsigned)(32 * LDV * 2), 0)); } while (0)
; #define ATT_WRITE_K(so) do { *(bf16x8*)(K_lds + (so) + kswz<DQK>(kr, kc * 2)) = sk0; if constexpr (DQK == 128) *(bf16x8*)(K_lds + (so) + kswz<DQK>(32 + kr, kc * 2)) = sk1; } while (0)
;     ...
;   for (int t = 0; t + 1 < NT; ++t) {
;     if constexpr (ABL & 1) { u32x4 w0 = {cvtpk(p0[0], p0[1]), cvtpk(p0[2], p0[3]), cvtpk(p0[4], p0[5]), cvtpk(p0[6], p0[7])}, w1 = {cvtpk(p0[8], p0[9]), cvtpk(p0[10], p0[11]), cvtpk(p0[12], p0[13]), cvtpk(p0[14], p0[15])};
;         u32x4 w2 = {cvtpk(p1[0], p1[1]), cvtpk(p1[2], p1[3]), cvtpk(p1[4], p1[5]), cvtpk(p1[6], p1[7])}, w3 = {cvtpk(p1[8], p1[9]), cvtpk(p1[10], p1[11]), cvtpk(p1[12], p1[13]), cvtpk(p1[14], p1[15])};
;         pa0 = *reinterpret_cast<bf16x8*>(&w0); pa1 = *reinterpret_cast<bf16x8*>(&w1); pa2 = *reinterpret_cast<bf16x8*>(&w2); pa3 = *reinterpret_cast<bf16x8*>(&w3); }
;     else { ATT_SOFTMAX(t == 0); }
;     if constexpr (!(ABL & 4)) { ATT_WRITE_K(k2); ATT_WRITE_V(v1); }
;     ATT_SBAR();
; #pragma unroll
;     for (int ks = 0; ks < 4; ++ks) ATT_VPAIR(va, v0, 0, ks);
;     asm volatile("s_waitcnt lgkmcnt(8)" ::: "memory"); ATT_BAR();
;     ATT_XSECTION(true);
;     if constexpr (!(ABL & 4)) { const int tk = (t + 3 < NT) ? t + 3 : NT - 1, tv = (t + 2 < NT) ? t + 2 : NT - 1; ATT_LOAD_K(tk); ATT_LOAD_V(tv); }
;     ATT_BAR();
;     { const int tk_ = k0; k0 = k1; k1 = k2; k2 = tk_; const int tv_ = v0; v0 = v1; v1 = v2; v2 = tv_; }
	s_setprio 2
	s_waitcnt lgkmcnt(3)
	v_mfma_f32_32x32x16_bf16 v[98:113], v[152:155], v[136:139], v[82:97]
	ds_read_b128 v[180:183], v249 offset:49216
	s_waitcnt lgkmcnt(3)
	v_mfma_f32_32x32x16_bf16 v[114:129], v[156:159], v[136:139], v[82:97]
	ds_read_b128 v[186:189], v249 offset:53824
	v_add_u32_e32 v248, s37, v131
	s_waitcnt lgkmcnt(3)
	v_mfma_f32_32x32x16_bf16 v[98:113], v[160:163], v[140:143], v[98:113]
	ds_read_b128 v[190:193], v249 offset:49248
	ds_read_b64_tr_b16 v[198:199], v248
	ds_read_b64_tr_b16 v[200:201], v248 offset:2048
	s_waitcnt lgkmcnt(5)
	v_mfma_f32_32x32x16_bf16 v[114:129], v[176:179], v[140:143], v[114:129]
	ds_read_b128 v[194:197], v249 offset:53856
	ds_read_b64_tr_b16 v[212:213], v248 offset:4096
	ds_read_b64_tr_b16 v[214:215], v248 offset:6144
	s_waitcnt lgkmcnt(7)
	v_mfma_f32_32x32x16_bf16 v[98:113], v[180:183], v[144:147], v[98:113]
	ds_read_b64_tr_b16 v[216:217], v248 offset:8192
	ds_read_b64_tr_b16 v[218:219], v248 offset:10240
	s_waitcnt lgkmcnt(8)
	v_mfma_f32_32x32x16_bf16 v[114:129], v[186:189], v[144:147], v[114:129]
	ds_read_b64_tr_b16 v[220:221], v248 offset:12288
	ds_read_b64_tr_b16 v[222:223], v248 offset:14336
	s_waitcnt lgkmcnt(9)
	v_mfma_f32_32x32x16_bf16 v[98:113], v[190:193], v[148:151], v[98:113]
	s_waitcnt lgkmcnt(6)
	v_mfma_f32_32x32x16_bf16 v[114:129], v[194:197], v[148:151], v[114:129]
	v_mfma_f32_32x32x16_bf16 v[66:81], v[18:21], v[198:201], v[66:81]
	ds_read_b64_tr_b16 v[236:237], v248 offset:512
	ds_read_b64_tr_b16 v[238:239], v248 offset:2560
	s_waitcnt lgkmcnt(6)
	v_mfma_f32_32x32x16_bf16 v[66:81], v[22:25], v[212:215], v[66:81]
	ds_read_b64_tr_b16 v[198:199], v248 offset:4608
	ds_read_b64_tr_b16 v[200:201], v248 offset:6656
	s_waitcnt lgkmcnt(6)
	v_mfma_f32_32x32x16_bf16 v[66:81], v[26:29], v[216:219], v[66:81]
	ds_read_b64_tr_b16 v[212:213], v248 offset:8704
	ds_read_b64_tr_b16 v[214:215], v248 offset:10752
	s_waitcnt lgkmcnt(6)
	v_mfma_f32_32x32x16_bf16 v[66:81], v[30:33], v[220:223], v[66:81]
	ds_read_b64_tr_b16 v[216:217], v248 offset:12800
	ds_read_b64_tr_b16 v[218:219], v248 offset:14848
	v_max3_f32 v249, v98, v99, v100
	s_waitcnt lgkmcnt(6)
	v_mfma_f32_32x32x16_bf16 v[50:65], v[18:21], v[236:239], v[50:65]
	ds_read_b64_tr_b16 v[220:221], v248 offset:1024
	ds_read_b64_tr_b16 v[222:223], v248 offset:3072
	v_max3_f32 v174, v114, v115, v116
	s_waitcnt lgkmcnt(6)
	v_mfma_f32_32x32x16_bf16 v[50:65], v[22:25], v[198:201], v[50:65]
	ds_read_b64_tr_b16 v[236:237], v248 offset:5120
	ds_read_b64_tr_b16 v[238:239], v248 offset:7168
	v_max3_f32 v249, v249, v101, v102
	s_waitcnt lgkmcnt(6)
	v_mfma_f32_32x32x16_bf16 v[50:65], v[26:29], v[212:215], v[50:65]
	ds_read_b64_tr_b16 v[198:199], v248 offset:9216
	ds_read_b64_tr_b16 v[200:201], v248 offset:11264
	v_max3_f32 v174, v174, v117, v118
	s_waitcnt lgkmcnt(6)
	v_mfma_f32_32x32x16_bf16 v[50:65], v[30:33], v[216:219], v[50:65]
	ds_read_b64_tr_b16 v[212:213], v248 offset:13312
	ds_read_b64_tr_b16 v[214:215], v248 offset:15360
	v_max3_f32 v249, v249, v103, v104
	s_waitcnt lgkmcnt(6)
	v_mfma_f32_32x32x16_bf16 v[34:49], v[18:21], v[220:223], v[34:49]
	ds_read_b64_tr_b16 v[216:217], v248 offset:1536
	ds_read_b64_tr_b16 v[218:219], v248 offset:3584
	v_max3_f32 v174, v174, v119, v120
	s_waitcnt lgkmcnt(6)
	v_mfma_f32_32x32x16_bf16 v[34:49], v[22:25], v[236:239], v[34:49]
	ds_read_b64_tr_b16 v[220:221], v248 offset:5632
	ds_read_b64_tr_b16 v[222:223], v248 offset:7680
	v_max3_f32 v249, v249, v105, v106
	s_waitcnt lgkmcnt(6)
	v_mfma_f32_32x32x16_bf16 v[34:49], v[26:29], v[198:201], v[34:49]
	ds_read_b64_tr_b16 v[236:237], v248 offset:9728
	ds_read_b64_tr_b16 v[238:239], v248 offset:11776
	v_max3_f32 v174, v174, v121, v122
	s_waitcnt lgkmcnt(6)
	v_mfma_f32_32x32x16_bf16 v[34:49], v[30:33], v[212:215], v[34:49]
	ds_read_b64_tr_b16 v[198:199], v248 offset:13824
	ds_read_b64_tr_b16 v[200:201], v248 offset:15872
	v_max3_f32 v249, v249, v107, v108
	s_waitcnt lgkmcnt(6)
	v_mfma_f32_32x32x16_bf16 v[2:17], v[18:21], v[216:219], v[2:17]
	v_max3_f32 v174, v174, v123, v124
	s_min_u32 s14, s90, 0x7c
	s_lshl_b32 s14, s14, 17
	s_add_i32 s19, s14, 0x60000
	s_add_i32 s92, s36, 0xffff0000
	s_mov_b32 s14, s10
	s_mov_b32 s15, s11
	buffer_load_dwordx4 v[224:227], v171, s[8:11], s19 offen
	s_waitcnt lgkmcnt(4)
	v_mfma_f32_32x32x16_bf16 v[2:17], v[22:25], v[220:223], v[2:17]
	v_max3_f32 v249, v249, v109, v110
	buffer_load_dwordx4 v[228:231], v172, s[12:15], s92 offen
	s_waitcnt lgkmcnt(2)
	v_mfma_f32_32x32x16_bf16 v[2:17], v[26:29], v[236:239], v[2:17]
	v_max3_f32 v174, v174, v125, v126
	buffer_load_dwordx4 v[232:235], v172, s[12:15], s36 offen
	s_waitcnt lgkmcnt(0)
	v_mfma_f32_32x32x16_bf16 v[2:17], v[30:33], v[198:201], v[2:17]
	v_max3_f32 v249, v249, v111, v112
	v_mfma_f32_4x4x4_16b_bf16 v[240:243], v[18:19], v[132:133], v[240:243]
	v_max3_f32 v174, v174, v127, v128
	v_mfma_f32_4x4x4_16b_bf16 v[244:247], v[20:21], v[132:133], v[244:247]
	v_mfma_f32_4x4x4_16b_bf16 v[240:243], v[22:23], v[132:133], v[240:243]
	v_max_f32 v249, v249, v113
	v_mfma_f32_4x4x4_16b_bf16 v[244:247], v[24:25], v[132:133], v[244:247]
	v_mfma_f32_4x4x4_16b_bf16 v[240:243], v[26:27], v[132:133], v[240:243]
	v_max_f32 v174, v174, v129
	v_mfma_f32_4x4x4_16b_bf16 v[244:247], v[28:29], v[132:133], v[244:247]
	v_mfma_f32_4x4x4_16b_bf16 v[240:243], v[30:31], v[132:133], v[240:243]
	v_max_f32 v174, v174, v249
	v_mfma_f32_4x4x4_16b_bf16 v[244:247], v[32:33], v[132:133], v[244:247]
	s_setprio 0
	s_add_i32 s36, s36, 0x20000
	s_add_i32 s90, s90, 1
	s_cmpk_eq_i32 s90, 0x7e
	s_cbranch_scc1 .Lrot_exit_b2
	s_mov_b32 s14, s49
	s_mov_b32 s49, s51
	s_mov_b32 s51, s18
	s_mov_b32 s15, s50
	s_mov_b32 s50, s48
	s_mov_b32 s48, s37
	s_mov_b32 s37, s15
	s_mov_b32 s18, s14
	s_barrier
	s_branch .Lrot_head_b2
